# speedup vs baseline: 1.0216x; 1.0080x over previous
_Z9k_scatterPKiS0_S0_S0_PiS1_:
	v_mov_b32_e32 v50, v0
	s_load_dwordx4 s[4:7], s[0:1], 0x0
	s_load_dwordx2 s[12:13], s[0:1], 0x18
	s_load_dwordx2 s[14:15], s[0:1], 0x10
	s_mul_i32 s3, s2, 0x186a
	v_add_u32_e32 v2, s3, v0
	v_ashrrev_i32_e32 v3, 31, v2
	v_lshlrev_b64 v[4:5], 2, v[2:3]
	s_waitcnt lgkmcnt(0)
	v_mov_b32_e32 v31, 0
	v_mov_b32_e32 v33, 0
	v_lshlrev_b32_e32 v32, 2, v0
	v_cmp_gt_u32_e32 vcc, 0x187, v0
	s_and_saveexec_b64 s[10:11], vcc
	global_load_dword v31, v32, s[12:13]
	v_lshl_add_u32 v34, v0, 8, s2
	v_lshlrev_b32_e32 v34, 2, v34
	global_load_dword v33, v34, s[14:15]
	s_or_b64 exec, exec, s[10:11]
	v_lshl_add_u64 v[6:7], s[6:7], 0, v[4:5]
	v_lshl_add_u64 v[4:5], s[4:5], 0, v[4:5]
	global_load_dword v30, v[4:5], off
	v_add_u32_e32 v4, 0x400, v2
	v_ashrrev_i32_e32 v5, 31, v4
	v_lshlrev_b64 v[4:5], 2, v[4:5]
	global_load_dword v29, v[6:7], off
	v_lshl_add_u64 v[6:7], s[6:7], 0, v[4:5]
	v_lshl_add_u64 v[4:5], s[4:5], 0, v[4:5]
	global_load_dword v28, v[4:5], off
	v_add_u32_e32 v4, 0x800, v2
	v_ashrrev_i32_e32 v5, 31, v4
	v_lshlrev_b64 v[4:5], 2, v[4:5]
	global_load_dword v27, v[6:7], off
	v_lshl_add_u64 v[6:7], s[6:7], 0, v[4:5]
	v_lshl_add_u64 v[4:5], s[4:5], 0, v[4:5]
	global_load_dword v26, v[4:5], off
	v_add_u32_e32 v4, 0xc00, v2
	v_ashrrev_i32_e32 v5, 31, v4
	v_lshlrev_b64 v[4:5], 2, v[4:5]
	global_load_dword v25, v[6:7], off
	v_lshl_add_u64 v[6:7], s[6:7], 0, v[4:5]
	v_lshl_add_u64 v[4:5], s[4:5], 0, v[4:5]
	global_load_dword v24, v[4:5], off
	v_add_u32_e32 v4, 0x1000, v2
	v_ashrrev_i32_e32 v5, 31, v4
	v_add_u32_e32 v2, 0x1400, v2
	v_lshlrev_b64 v[4:5], 2, v[4:5]
	v_ashrrev_i32_e32 v3, 31, v2
	global_load_dword v23, v[6:7], off
	v_lshl_add_u64 v[6:7], s[6:7], 0, v[4:5]
	v_lshl_add_u64 v[4:5], s[4:5], 0, v[4:5]
	v_lshlrev_b64 v[2:3], 2, v[2:3]
	global_load_dword v22, v[4:5], off
	v_lshl_add_u64 v[4:5], s[6:7], 0, v[2:3]
	v_lshl_add_u64 v[2:3], s[4:5], 0, v[2:3]
	global_load_dword v21, v[6:7], off
	global_load_dword v18, v[4:5], off
	global_load_dword v19, v[2:3], off
	s_movk_i32 s8, 0x186a
	v_or_b32_e32 v2, 0x1800, v0
	v_cmp_gt_u32_e32 vcc, s8, v2
	v_add_u32_e32 v2, s3, v2
	v_mov_b32_e32 v1, -1
	v_ashrrev_i32_e32 v3, 31, v2
	s_and_saveexec_b64 s[8:9], vcc
	s_cbranch_execz .LBB1_2
	v_lshl_add_u64 v[4:5], v[2:3], 2, s[6:7]
	global_load_dword v1, v[4:5], off

.LBB1_4:
	s_or_b64 exec, exec, s[6:7]
	s_movk_i32 s3, 0x187
	v_cmp_gt_u32_e32 vcc, s3, v0
	v_lshlrev_b32_e32 v32, 2, v0
	v_mbcnt_lo_u32_b32 v2, -1, 0
	v_mbcnt_hi_u32_b32 v2, -1, v2
	v_and_b32_e32 v3, 64, v2
	v_add_u32_e32 v4, -1, v2
	v_cmp_lt_i32_e64 s[4:5], v4, v3
	v_and_b32_e32 v5, 63, v0
	v_add_u32_e32 v6, -2, v2
	v_cndmask_b32_e64 v4, v4, v2, s[4:5]
	v_lshlrev_b32_e32 v4, 2, v4
	s_waitcnt vmcnt(12)
	ds_bpermute_b32 v4, v4, v31
	v_cmp_ne_u32_e64 s[4:5], 0, v5
	s_load_dwordx2 s[6:7], s[0:1], 0x20
	v_lshrrev_b32_e32 v34, 6, v0
	s_waitcnt lgkmcnt(0)
	v_cndmask_b32_e64 v4, 0, v4, s[4:5]
	v_cmp_lt_i32_e64 s[4:5], v6, v3
	v_add_u32_e32 v4, v4, v31
	s_nop 0
	v_cndmask_b32_e64 v6, v6, v2, s[4:5]
	v_lshlrev_b32_e32 v6, 2, v6
	ds_bpermute_b32 v6, v6, v4
	v_cmp_lt_u32_e64 s[4:5], 1, v5
	s_waitcnt lgkmcnt(0)
	s_nop 0
	v_cndmask_b32_e64 v6, 0, v6, s[4:5]
	v_add_u32_e32 v4, v6, v4
	v_add_u32_e32 v6, -4, v2
	v_cmp_lt_i32_e64 s[4:5], v6, v3
	s_nop 1
	v_cndmask_b32_e64 v6, v6, v2, s[4:5]
	v_lshlrev_b32_e32 v6, 2, v6
	ds_bpermute_b32 v6, v6, v4
	v_cmp_lt_u32_e64 s[4:5], 3, v5
	s_waitcnt lgkmcnt(0)
	s_nop 0
	v_cndmask_b32_e64 v6, 0, v6, s[4:5]
	v_add_u32_e32 v4, v6, v4
	v_add_u32_e32 v6, -8, v2
	v_cmp_lt_i32_e64 s[4:5], v6, v3
	s_nop 1
	v_cndmask_b32_e64 v6, v6, v2, s[4:5]
	v_lshlrev_b32_e32 v6, 2, v6
	ds_bpermute_b32 v6, v6, v4
	v_cmp_lt_u32_e64 s[4:5], 7, v5
	s_waitcnt lgkmcnt(0)
	s_nop 0
	v_cndmask_b32_e64 v6, 0, v6, s[4:5]
	v_add_u32_e32 v4, v6, v4
	v_add_u32_e32 v6, -16, v2
	v_cmp_lt_i32_e64 s[4:5], v6, v3
	s_nop 1
	v_cndmask_b32_e64 v6, v6, v2, s[4:5]
	v_lshlrev_b32_e32 v6, 2, v6
	ds_bpermute_b32 v6, v6, v4
	v_cmp_lt_u32_e64 s[4:5], 15, v5
	s_waitcnt lgkmcnt(0)
	s_nop 0
	v_cndmask_b32_e64 v6, 0, v6, s[4:5]
	v_add_u32_e32 v4, v6, v4
	v_subrev_u32_e32 v6, 32, v2
	v_cmp_lt_i32_e64 s[4:5], v6, v3
	s_nop 1
	v_cndmask_b32_e64 v2, v6, v2, s[4:5]
	v_lshlrev_b32_e32 v2, 2, v2
	ds_bpermute_b32 v2, v2, v4
	v_cmp_lt_u32_e64 s[4:5], 31, v5
	s_waitcnt lgkmcnt(0)
	s_nop 0
	v_cndmask_b32_e64 v2, 0, v2, s[4:5]
	v_add_u32_e32 v35, v2, v4
	v_cmp_eq_u32_e64 s[4:5], 63, v5
	s_and_saveexec_b64 s[8:9], s[4:5]
	v_lshlrev_b32_e32 v2, 2, v34
	ds_write_b32 v2, v35 offset:1568
	s_or_b64 exec, exec, s[8:9]
	v_mov_b32_e32 v2, 0
	s_waitcnt lgkmcnt(0)
	s_barrier
	ds_read_b128 v[14:17], v2 offset:1568
	ds_read_b128 v[10:13], v2 offset:1584
	ds_read_b128 v[6:9], v2 offset:1600
	ds_read_b128 v[2:5], v2 offset:1616
	s_waitcnt lgkmcnt(0)
	s_barrier
	s_and_saveexec_b64 s[4:5], vcc
	s_cbranch_execz .LBB1_13
	v_cmp_lt_u32_e32 vcc, 63, v0
	s_movk_i32 s3, 0x7f
	v_sub_u32_e32 v31, v35, v31
	v_cndmask_b32_e32 v36, 0, v14, vcc
	v_cmp_lt_u32_e32 vcc, s3, v0
	s_movk_i32 s3, 0xbf
	v_add_u32_e32 v31, v36, v31
	v_cndmask_b32_e32 v37, 0, v15, vcc
	v_cmp_lt_u32_e32 vcc, s3, v0
	s_movk_i32 s3, 0xff
	s_cmp_lg_u32 s2, 0
	v_cndmask_b32_e32 v38, 0, v16, vcc
	v_cmp_lt_u32_e32 vcc, s3, v0
	s_movk_i32 s3, 0x13f
	v_add3_u32 v31, v31, v37, v38
	v_cndmask_b32_e32 v39, 0, v17, vcc
	v_cmp_lt_u32_e32 vcc, s3, v0
	s_movk_i32 s3, 0x17f
	s_nop 0
	v_cndmask_b32_e32 v40, 0, v10, vcc
	v_cmp_lt_u32_e32 vcc, s3, v0
	s_movk_i32 s3, 0x1bf
	v_add3_u32 v31, v31, v39, v40
	v_cndmask_b32_e32 v41, 0, v11, vcc
	v_cmp_lt_u32_e32 vcc, s3, v0
	s_movk_i32 s3, 0x1ff
	s_nop 0
	v_cndmask_b32_e32 v42, 0, v12, vcc
	v_cmp_lt_u32_e32 vcc, s3, v0
	s_movk_i32 s3, 0x23f
	v_add3_u32 v31, v31, v41, v42
	v_cndmask_b32_e32 v43, 0, v13, vcc
	v_cmp_lt_u32_e32 vcc, s3, v0
	s_movk_i32 s3, 0x27f
	s_nop 0
	v_cndmask_b32_e32 v44, 0, v6, vcc
	v_cmp_lt_u32_e32 vcc, s3, v0
	s_movk_i32 s3, 0x2bf
	v_add3_u32 v31, v31, v43, v44
	v_cndmask_b32_e32 v45, 0, v7, vcc
	v_cmp_lt_u32_e32 vcc, s3, v0
	s_movk_i32 s3, 0x2ff
	s_nop 0
	v_cndmask_b32_e32 v46, 0, v8, vcc
	v_cmp_lt_u32_e32 vcc, s3, v0
	s_movk_i32 s3, 0x33f
	v_add3_u32 v31, v31, v45, v46
	v_cndmask_b32_e32 v47, 0, v9, vcc
	v_cmp_lt_u32_e32 vcc, s3, v0
	s_movk_i32 s3, 0x37f
	s_nop 0
	v_cndmask_b32_e32 v48, 0, v2, vcc
	v_cmp_lt_u32_e32 vcc, s3, v0
	v_add3_u32 v31, v31, v47, v48
	s_nop 0
	v_cndmask_b32_e32 v49, 0, v3, vcc
	v_cmp_eq_u32_e32 vcc, 15, v34
	s_nop 1
	v_cndmask_b32_e32 v34, 0, v4, vcc
	v_add3_u32 v31, v31, v49, v34
	v_add_u32_e32 v33, v31, v33
	ds_write_b32 v32, v33
	ds_write_b32 v32, v33 offset:2048
	s_cbranch_scc1 .LBB1_13
	global_store_dword v32, v31, s[6:7]

.LBB1_15:
	s_or_b64 exec, exec, s[2:3]
	s_waitcnt vmcnt(0)
	v_lshlrev_b32_e32 v20, 8, v20
	s_waitcnt lgkmcnt(0)
	s_barrier
	v_mov_b32_e32 v51, 1
	s_mov_b32 s4, 0x6050400
	s_movk_i32 s5, 0xff
	v_cmp_lt_i32_e64 s[16:17], -1, v29
	v_lshrrev_b32_e32 v52, 6, v29
	v_and_b32_e32 v52, 0x3fffffc, v52
	v_cmp_lt_i32_e64 s[18:19], -1, v27
	v_lshrrev_b32_e32 v53, 6, v27
	v_and_b32_e32 v53, 0x3fffffc, v53
	v_cmp_lt_i32_e64 s[20:21], -1, v25
	v_lshrrev_b32_e32 v54, 6, v25
	v_and_b32_e32 v54, 0x3fffffc, v54
	v_cmp_lt_i32_e64 s[22:23], -1, v23
	v_lshrrev_b32_e32 v55, 6, v23
	v_and_b32_e32 v55, 0x3fffffc, v55
	v_cmp_lt_i32_e64 s[24:25], -1, v21
	v_lshrrev_b32_e32 v56, 6, v21
	v_and_b32_e32 v56, 0x3fffffc, v56
	v_cmp_lt_i32_e64 s[26:27], -1, v18
	v_lshrrev_b32_e32 v57, 6, v18
	v_and_b32_e32 v57, 0x3fffffc, v57
	v_cmp_lt_i32_e64 s[28:29], -1, v1
	v_lshrrev_b32_e32 v58, 6, v1
	v_and_b32_e32 v58, 0x3fffffc, v58
	s_mov_b64 exec, s[16:17]
	ds_add_rtn_u32 v60, v52, v51
	ds_read_b32 v68, v52 offset:2048
	s_mov_b64 exec, s[18:19]
	ds_add_rtn_u32 v61, v53, v51
	ds_read_b32 v69, v53 offset:2048
	s_mov_b64 exec, s[20:21]
	ds_add_rtn_u32 v62, v54, v51
	ds_read_b32 v70, v54 offset:2048
	s_mov_b64 exec, s[22:23]
	ds_add_rtn_u32 v63, v55, v51
	ds_read_b32 v71, v55 offset:2048
	s_mov_b64 exec, s[24:25]
	ds_add_rtn_u32 v64, v56, v51
	ds_read_b32 v72, v56 offset:2048
	s_mov_b64 exec, s[26:27]
	ds_add_rtn_u32 v65, v57, v51
	ds_read_b32 v73, v57 offset:2048
	s_mov_b64 exec, s[28:29]
	ds_add_rtn_u32 v66, v58, v51
	ds_read_b32 v74, v58 offset:2048
	s_mov_b64 exec, -1
	v_perm_b32 v76, v30, v29, s4
	v_perm_b32 v77, v28, v27, s4
	v_perm_b32 v78, v26, v25, s4
	v_perm_b32 v79, v24, v23, s4
	v_perm_b32 v80, v22, v21, s4
	v_perm_b32 v81, v19, v18, s4
	v_and_or_b32 v82, v1, s5, v20
	s_waitcnt lgkmcnt(0)
	v_sub_u32_e32 v68, v60, v68
	v_lshlrev_b32_e32 v52, 5, v52
	v_lshl_add_u32 v52, v68, 2, v52
	v_cmp_gt_u32_e64 s[30:31], 32, v68
	s_and_b64 s[32:33], s[16:17], s[30:31]
	s_andn2_b64 s[34:35], s[16:17], s[30:31]
	s_mov_b64 exec, s[32:33]
	ds_write_b32 v52, v76 offset:4096
	s_mov_b64 exec, s[34:35]
	s_cbranch_execz .Lsc2_o0
	v_ashrrev_i32_e32 v3, 31, v60
	v_mov_b32_e32 v2, v60
	v_lshl_add_u64 v[2:3], v[2:3], 2, s[0:1]
	global_store_dword v[2:3], v76, off
.Lsc2_o0:
	s_mov_b64 exec, -1
	v_sub_u32_e32 v69, v61, v69
	v_lshlrev_b32_e32 v53, 5, v53
	v_lshl_add_u32 v53, v69, 2, v53
	v_cmp_gt_u32_e64 s[30:31], 32, v69
	s_and_b64 s[32:33], s[18:19], s[30:31]
	s_andn2_b64 s[34:35], s[18:19], s[30:31]
	s_mov_b64 exec, s[32:33]
	ds_write_b32 v53, v77 offset:4096
	s_mov_b64 exec, s[34:35]
	s_cbranch_execz .Lsc2_o1
	v_ashrrev_i32_e32 v3, 31, v61
	v_mov_b32_e32 v2, v61
	v_lshl_add_u64 v[2:3], v[2:3], 2, s[0:1]
	global_store_dword v[2:3], v77, off
.Lsc2_o1:
	s_mov_b64 exec, -1
	v_sub_u32_e32 v70, v62, v70
	v_lshlrev_b32_e32 v54, 5, v54
	v_lshl_add_u32 v54, v70, 2, v54
	v_cmp_gt_u32_e64 s[30:31], 32, v70
	s_and_b64 s[32:33], s[20:21], s[30:31]
	s_andn2_b64 s[34:35], s[20:21], s[30:31]
	s_mov_b64 exec, s[32:33]
	ds_write_b32 v54, v78 offset:4096
	s_mov_b64 exec, s[34:35]
	s_cbranch_execz .Lsc2_o2
	v_ashrrev_i32_e32 v3, 31, v62
	v_mov_b32_e32 v2, v62
	v_lshl_add_u64 v[2:3], v[2:3], 2, s[0:1]
	global_store_dword v[2:3], v78, off
.Lsc2_o2:
	s_mov_b64 exec, -1
	v_sub_u32_e32 v71, v63, v71
	v_lshlrev_b32_e32 v55, 5, v55
	v_lshl_add_u32 v55, v71, 2, v55
	v_cmp_gt_u32_e64 s[30:31], 32, v71
	s_and_b64 s[32:33], s[22:23], s[30:31]
	s_andn2_b64 s[34:35], s[22:23], s[30:31]
	s_mov_b64 exec, s[32:33]
	ds_write_b32 v55, v79 offset:4096
	s_mov_b64 exec, s[34:35]
	s_cbranch_execz .Lsc2_o3
	v_ashrrev_i32_e32 v3, 31, v63
	v_mov_b32_e32 v2, v63
	v_lshl_add_u64 v[2:3], v[2:3], 2, s[0:1]
	global_store_dword v[2:3], v79, off
.Lsc2_o3:
	s_mov_b64 exec, -1
	v_sub_u32_e32 v72, v64, v72
	v_lshlrev_b32_e32 v56, 5, v56
	v_lshl_add_u32 v56, v72, 2, v56
	v_cmp_gt_u32_e64 s[30:31], 32, v72
	s_and_b64 s[32:33], s[24:25], s[30:31]
	s_andn2_b64 s[34:35], s[24:25], s[30:31]
	s_mov_b64 exec, s[32:33]
	ds_write_b32 v56, v80 offset:4096
	s_mov_b64 exec, s[34:35]
	s_cbranch_execz .Lsc2_o4
	v_ashrrev_i32_e32 v3, 31, v64
	v_mov_b32_e32 v2, v64
	v_lshl_add_u64 v[2:3], v[2:3], 2, s[0:1]
	global_store_dword v[2:3], v80, off
.Lsc2_o4:
	s_mov_b64 exec, -1
	v_sub_u32_e32 v73, v65, v73
	v_lshlrev_b32_e32 v57, 5, v57
	v_lshl_add_u32 v57, v73, 2, v57
	v_cmp_gt_u32_e64 s[30:31], 32, v73
	s_and_b64 s[32:33], s[26:27], s[30:31]
	s_andn2_b64 s[34:35], s[26:27], s[30:31]
	s_mov_b64 exec, s[32:33]
	ds_write_b32 v57, v81 offset:4096
	s_mov_b64 exec, s[34:35]
	s_cbranch_execz .Lsc2_o5
	v_ashrrev_i32_e32 v3, 31, v65
	v_mov_b32_e32 v2, v65
	v_lshl_add_u64 v[2:3], v[2:3], 2, s[0:1]
	global_store_dword v[2:3], v81, off
.Lsc2_o5:
	s_mov_b64 exec, -1
	v_sub_u32_e32 v74, v66, v74
	v_lshlrev_b32_e32 v58, 5, v58
	v_lshl_add_u32 v58, v74, 2, v58
	v_cmp_gt_u32_e64 s[30:31], 32, v74
	s_and_b64 s[32:33], s[28:29], s[30:31]
	s_andn2_b64 s[34:35], s[28:29], s[30:31]
	s_mov_b64 exec, s[32:33]
	ds_write_b32 v58, v82 offset:4096
	s_mov_b64 exec, s[34:35]
	s_cbranch_execz .Lsc2_o6
	v_ashrrev_i32_e32 v3, 31, v66
	v_mov_b32_e32 v2, v66
	v_lshl_add_u64 v[2:3], v[2:3], 2, s[0:1]
	global_store_dword v[2:3], v82, off
.Lsc2_o6:
	s_mov_b64 exec, -1
	s_mov_b64 exec, -1
	v_lshlrev_b32_e32 v84, 2, v50
	v_lshrrev_b32_e32 v85, 5, v50
	v_lshlrev_b32_e32 v85, 2, v85
	v_and_b32_e32 v86, 31, v50
	s_movk_i32 s36, 0xe0
	v_cmp_gt_u32_e64 s[36:37], s36, v50
	s_waitcnt lgkmcnt(0)
	s_barrier
	ds_read_b32 v88, v85 offset:0
	ds_read_b32 v95, v85 offset:2048
	ds_read_b32 v102, v84 offset:4096
	ds_read_b32 v89, v85 offset:128
	ds_read_b32 v96, v85 offset:2176
	ds_read_b32 v103, v84 offset:8192
	ds_read_b32 v90, v85 offset:256
	ds_read_b32 v97, v85 offset:2304
	ds_read_b32 v104, v84 offset:12288
	ds_read_b32 v91, v85 offset:384
	ds_read_b32 v98, v85 offset:2432
	ds_read_b32 v105, v84 offset:16384
	ds_read_b32 v92, v85 offset:512
	ds_read_b32 v99, v85 offset:2560
	ds_read_b32 v106, v84 offset:20480
	s_waitcnt lgkmcnt(0)
	v_sub_u32_e32 v88, v88, v95
	v_cmp_lt_u32_e64 s[30:31], v86, v88
	v_add_lshl_u32 v95, v95, v86, 2
	s_mov_b64 exec, s[30:31]
	global_store_dword v95, v102, s[0:1]
	s_mov_b64 exec, -1
	v_sub_u32_e32 v89, v89, v96
	v_cmp_lt_u32_e64 s[30:31], v86, v89
	v_add_lshl_u32 v96, v96, v86, 2
	s_mov_b64 exec, s[30:31]
	global_store_dword v96, v103, s[0:1]
	s_mov_b64 exec, -1
	v_sub_u32_e32 v90, v90, v97
	v_cmp_lt_u32_e64 s[30:31], v86, v90
	v_add_lshl_u32 v97, v97, v86, 2
	s_mov_b64 exec, s[30:31]
	global_store_dword v97, v104, s[0:1]
	s_mov_b64 exec, -1
	v_sub_u32_e32 v91, v91, v98
	v_cmp_lt_u32_e64 s[30:31], v86, v91
	v_add_lshl_u32 v98, v98, v86, 2
	s_mov_b64 exec, s[30:31]
	global_store_dword v98, v105, s[0:1]
	s_mov_b64 exec, -1
	v_sub_u32_e32 v92, v92, v99
	v_cmp_lt_u32_e64 s[30:31], v86, v92
	v_add_lshl_u32 v99, v99, v86, 2
	s_mov_b64 exec, s[30:31]
	global_store_dword v99, v106, s[0:1]
	s_mov_b64 exec, -1
	ds_read_b32 v88, v85 offset:640
	ds_read_b32 v95, v85 offset:2688
	ds_read_b32 v102, v84 offset:24576
	ds_read_b32 v89, v85 offset:768
	ds_read_b32 v96, v85 offset:2816
	ds_read_b32 v103, v84 offset:28672
	ds_read_b32 v90, v85 offset:896
	ds_read_b32 v97, v85 offset:2944
	ds_read_b32 v104, v84 offset:32768
	ds_read_b32 v91, v85 offset:1024
	ds_read_b32 v98, v85 offset:3072
	ds_read_b32 v105, v84 offset:36864
	ds_read_b32 v92, v85 offset:1152
	ds_read_b32 v99, v85 offset:3200
	ds_read_b32 v106, v84 offset:40960
	s_waitcnt lgkmcnt(0)
	v_sub_u32_e32 v88, v88, v95
	v_cmp_lt_u32_e64 s[30:31], v86, v88
	v_add_lshl_u32 v95, v95, v86, 2
	s_mov_b64 exec, s[30:31]
	global_store_dword v95, v102, s[0:1]
	s_mov_b64 exec, -1
	v_sub_u32_e32 v89, v89, v96
	v_cmp_lt_u32_e64 s[30:31], v86, v89
	v_add_lshl_u32 v96, v96, v86, 2
	s_mov_b64 exec, s[30:31]
	global_store_dword v96, v103, s[0:1]
	s_mov_b64 exec, -1
	v_sub_u32_e32 v90, v90, v97
	v_cmp_lt_u32_e64 s[30:31], v86, v90
	v_add_lshl_u32 v97, v97, v86, 2
	s_mov_b64 exec, s[30:31]
	global_store_dword v97, v104, s[0:1]
	s_mov_b64 exec, -1
	v_sub_u32_e32 v91, v91, v98
	v_cmp_lt_u32_e64 s[30:31], v86, v91
	v_add_lshl_u32 v98, v98, v86, 2
	s_mov_b64 exec, s[30:31]
	global_store_dword v98, v105, s[0:1]
	s_mov_b64 exec, -1
	v_sub_u32_e32 v92, v92, v99
	v_cmp_lt_u32_e64 s[30:31], v86, v92
	v_add_lshl_u32 v99, v99, v86, 2
	s_mov_b64 exec, s[30:31]
	global_store_dword v99, v106, s[0:1]
	s_mov_b64 exec, -1
	ds_read_b32 v88, v85 offset:1280
	ds_read_b32 v95, v85 offset:3328
	ds_read_b32 v102, v84 offset:45056
	ds_read_b32 v89, v85 offset:1408
	ds_read_b32 v96, v85 offset:3456
	ds_read_b32 v103, v84 offset:49152
	ds_read_b32 v90, v85 offset:1536
	ds_read_b32 v97, v85 offset:3584
	ds_read_b32 v104, v84 offset:53248
	s_waitcnt lgkmcnt(0)
	v_sub_u32_e32 v88, v88, v95
	v_cmp_lt_u32_e64 s[30:31], v86, v88
	v_add_lshl_u32 v95, v95, v86, 2
	s_mov_b64 exec, s[30:31]
	global_store_dword v95, v102, s[0:1]
	s_mov_b64 exec, -1
	v_sub_u32_e32 v89, v89, v96
	v_cmp_lt_u32_e64 s[30:31], v86, v89
	v_add_lshl_u32 v96, v96, v86, 2
	s_mov_b64 exec, s[30:31]
	global_store_dword v96, v103, s[0:1]
	s_mov_b64 exec, -1
	v_sub_u32_e32 v90, v90, v97
	v_cmp_lt_u32_e64 s[30:31], v86, v90
	v_add_lshl_u32 v97, v97, v86, 2
	s_and_b64 s[30:31], s[30:31], s[36:37]
	s_mov_b64 exec, s[30:31]
	global_store_dword v97, v104, s[0:1]
	s_mov_b64 exec, -1
	s_endpgm

	.amdhsa_kernel _Z9k_scatterPKiS0_S0_S0_PiS1_
		.amdhsa_group_segment_fixed_size 54144
		.amdhsa_private_segment_fixed_size 0
		.amdhsa_kernarg_size 48
		.amdhsa_user_sgpr_count 2
		.amdhsa_user_sgpr_dispatch_ptr 0
		.amdhsa_user_sgpr_queue_ptr 0
		.amdhsa_user_sgpr_kernarg_segment_ptr 1
		.amdhsa_user_sgpr_dispatch_id 0
		.amdhsa_user_sgpr_kernarg_preload_length 0
		.amdhsa_user_sgpr_kernarg_preload_offset 0
		.amdhsa_user_sgpr_private_segment_size 0
		.amdhsa_uses_dynamic_stack 0
		.amdhsa_enable_private_segment 0
		.amdhsa_system_sgpr_workgroup_id_x 1
		.amdhsa_system_sgpr_workgroup_id_y 0
		.amdhsa_system_sgpr_workgroup_id_z 0
		.amdhsa_system_sgpr_workgroup_info 0
		.amdhsa_system_vgpr_workitem_id 0
		.amdhsa_next_free_vgpr 112
		.amdhsa_next_free_sgpr 40
		.amdhsa_accum_offset 112
		.amdhsa_reserve_vcc 1
		.amdhsa_float_round_mode_32 0
		.amdhsa_float_round_mode_16_64 0
		.amdhsa_float_denorm_mode_32 3
		.amdhsa_float_denorm_mode_16_64 3
		.amdhsa_dx10_clamp 1
		.amdhsa_ieee_mode 1
		.amdhsa_fp16_overflow 0
		.amdhsa_tg_split 0
		.amdhsa_exception_fp_ieee_invalid_op 0
		.amdhsa_exception_fp_denorm_src 0
		.amdhsa_exception_fp_ieee_div_zero 0
		.amdhsa_exception_fp_ieee_overflow 0
		.amdhsa_exception_fp_ieee_underflow 0
		.amdhsa_exception_fp_ieee_inexact 0
		.amdhsa_exception_int_div_zero 0
	.end_amdhsa_kernel

amdhsa.kernels:
  - .agpr_count:     0
    .args:
      - .actual_access:  read_only
        .address_space:  global
        .offset:         0
        .size:           8
        .value_kind:     global_buffer
      - .actual_access:  write_only
        .address_space:  global
        .offset:         8
        .size:           8
        .value_kind:     global_buffer
      - .actual_access:  read_only
        .address_space:  global
        .offset:         16
        .size:           8
        .value_kind:     global_buffer
      - .actual_access:  read_only
        .address_space:  global
        .offset:         24
        .size:           8
        .value_kind:     global_buffer
      - .actual_access:  read_only
        .address_space:  global
        .offset:         32
        .size:           8
        .value_kind:     global_buffer
      - .actual_access:  read_only
        .address_space:  global
        .offset:         40
        .size:           8
        .value_kind:     global_buffer
      - .actual_access:  read_only
        .address_space:  global
        .offset:         48
        .size:           8
        .value_kind:     global_buffer
      - .actual_access:  read_only
        .address_space:  global
        .offset:         56
        .size:           8
        .value_kind:     global_buffer
      - .actual_access:  read_only
        .address_space:  global
        .offset:         64
        .size:           8
        .value_kind:     global_buffer
      - .actual_access:  read_only
        .address_space:  global
        .offset:         72
        .size:           8
        .value_kind:     global_buffer
      - .actual_access:  read_only
        .address_space:  global
        .offset:         80
        .size:           8
        .value_kind:     global_buffer
      - .actual_access:  write_only
        .address_space:  global
        .offset:         88
        .size:           8
        .value_kind:     global_buffer
      - .actual_access:  write_only
        .address_space:  global
        .offset:         96
        .size:           8
        .value_kind:     global_buffer
      - .actual_access:  write_only
        .address_space:  global
        .offset:         104
        .size:           8
        .value_kind:     global_buffer
      - .actual_access:  write_only
        .address_space:  global
        .offset:         112
        .size:           8
        .value_kind:     global_buffer
      - .actual_access:  write_only
        .address_space:  global
        .offset:         120
        .size:           8
        .value_kind:     global_buffer
    .group_segment_fixed_size: 1564
    .kernarg_segment_align: 8
    .kernarg_segment_size: 128
    .language:       OpenCL C
    .language_version:
      - 2
      - 0
    .max_flat_workgroup_size: 1024
    .name:           _Z6k_pre1PKiPiPKfS3_S3_S3_S3_S3_S3_S3_S3_PDF16_S4_S4_PfS5_
    .private_segment_fixed_size: 0
    .sgpr_count:     26
    .sgpr_spill_count: 0
    .symbol:         _Z6k_pre1PKiPiPKfS3_S3_S3_S3_S3_S3_S3_S3_PDF16_S4_S4_PfS5_.kd
    .uniform_work_group_size: 1
    .uses_dynamic_stack: false
    .vgpr_count:     64
    .vgpr_spill_count: 0
    .wavefront_size: 64
  - .agpr_count:     0
    .args:
      - .actual_access:  read_only
        .address_space:  global
        .offset:         0
        .size:           8
        .value_kind:     global_buffer
      - .actual_access:  read_only
        .address_space:  global
        .offset:         8
        .size:           8
        .value_kind:     global_buffer
      - .actual_access:  read_only
        .address_space:  global
        .offset:         16
        .size:           8
        .value_kind:     global_buffer
      - .actual_access:  read_only
        .address_space:  global
        .offset:         24
        .size:           8
        .value_kind:     global_buffer
      - .actual_access:  write_only
        .address_space:  global
        .offset:         32
        .size:           8
        .value_kind:     global_buffer
      - .actual_access:  write_only
        .address_space:  global
        .offset:         40
        .size:           8
        .value_kind:     global_buffer
    .group_segment_fixed_size: 54144
    .kernarg_segment_align: 8
    .kernarg_segment_size: 48
    .language:       OpenCL C
    .language_version:
      - 2
      - 0
    .max_flat_workgroup_size: 1024
    .name:           _Z9k_scatterPKiS0_S0_S0_PiS1_
    .private_segment_fixed_size: 0
    .sgpr_count: 46
    .sgpr_spill_count: 0
    .symbol:         _Z9k_scatterPKiS0_S0_S0_PiS1_.kd
    .uniform_work_group_size: 1
    .uses_dynamic_stack: false
    .vgpr_count: 112
    .vgpr_spill_count: 0
    .wavefront_size: 64
  - .agpr_count:     0
    .args:
      - .actual_access:  read_only
        .address_space:  global
        .offset:         0
        .size:           8
        .value_kind:     global_buffer
      - .actual_access:  read_only
        .address_space:  global
        .offset:         8
        .size:           8
        .value_kind:     global_buffer
      - .actual_access:  write_only
        .address_space:  global
        .offset:         16
        .size:           8
        .value_kind:     global_buffer
      - .actual_access:  write_only
        .address_space:  global
        .offset:         24
        .size:           8
        .value_kind:     global_buffer
      - .actual_access:  read_only
        .address_space:  global
        .offset:         32
        .size:           8
        .value_kind:     global_buffer
      - .actual_access:  read_only
        .address_space:  global
        .offset:         40
        .size:           8
        .value_kind:     global_buffer
      - .actual_access:  read_only
        .address_space:  global
        .offset:         48
        .size:           8
        .value_kind:     global_buffer
      - .actual_access:  read_only
        .address_space:  global
        .offset:         56
        .size:           8
        .value_kind:     global_buffer
      - .actual_access:  write_only
        .address_space:  global
        .offset:         64
        .size:           8
        .value_kind:     global_buffer
      - .actual_access:  write_only
        .address_space:  global
        .offset:         72
        .size:           8
        .value_kind:     global_buffer
      - .actual_access:  write_only
        .address_space:  global
        .offset:         80
        .size:           8
        .value_kind:     global_buffer
    .group_segment_fixed_size: 60224
    .kernarg_segment_align: 8
    .kernarg_segment_size: 88
    .language:       OpenCL C
    .language_version:
      - 2
      - 0
    .max_flat_workgroup_size: 1024
    .name:           _Z5k_csrPKiS0_PiS1_PKfS3_S3_S3_PDF16_P15HIP_vector_typeIfLj4EES7_
    .private_segment_fixed_size: 0
    .sgpr_count:     86
    .sgpr_spill_count: 0
    .symbol:         _Z5k_csrPKiS0_PiS1_PKfS3_S3_S3_PDF16_P15HIP_vector_typeIfLj4EES7_.kd
    .uniform_work_group_size: 1
    .uses_dynamic_stack: false
    .vgpr_count:     64
    .vgpr_spill_count: 0
    .wavefront_size: 64
  - .agpr_count:     0
    .args:
      - .actual_access:  read_only
        .address_space:  global
        .offset:         0
        .size:           8
        .value_kind:     global_buffer
      - .actual_access:  write_only
        .address_space:  global
        .offset:         8
        .size:           8
        .value_kind:     global_buffer
      - .actual_access:  write_only
        .address_space:  global
        .offset:         16
        .size:           8
        .value_kind:     global_buffer
    .group_segment_fixed_size: 16
    .kernarg_segment_align: 8
    .kernarg_segment_size: 24
    .language:       OpenCL C
    .language_version:
      - 2
      - 0
    .max_flat_workgroup_size: 256
    .name:           _Z6k_pre2PKiPiS1_
    .private_segment_fixed_size: 0
    .sgpr_count:     14
    .sgpr_spill_count: 0
    .symbol:         _Z6k_pre2PKiPiS1_.kd
    .uniform_work_group_size: 1
    .uses_dynamic_stack: false
    .vgpr_count:     14
    .vgpr_spill_count: 0
    .wavefront_size: 64
  - .agpr_count:     0
    .args:
      - .actual_access:  read_only
        .address_space:  global
        .offset:         0
        .size:           8
        .value_kind:     global_buffer
      - .actual_access:  read_only
        .address_space:  global
        .offset:         8
        .size:           8
        .value_kind:     global_buffer
      - .actual_access:  read_only
        .address_space:  global
        .offset:         16
        .size:           8
        .value_kind:     global_buffer
      - .actual_access:  read_only
        .address_space:  global
        .offset:         24
        .size:           8
        .value_kind:     global_buffer
      - .actual_access:  read_only
        .address_space:  global
        .offset:         32
        .size:           8
        .value_kind:     global_buffer
      - .actual_access:  write_only
        .address_space:  global
        .offset:         40
        .size:           8
        .value_kind:     global_buffer
    .group_segment_fixed_size: 1408
    .kernarg_segment_align: 8
    .kernarg_segment_size: 48
    .language:       OpenCL C
    .language_version:
      - 2
      - 0
    .max_flat_workgroup_size: 256
    .name:           _Z7k_finalPKfS0_S0_S0_S0_Pf
    .private_segment_fixed_size: 0
    .sgpr_count:     26
    .sgpr_spill_count: 0
    .symbol:         _Z7k_finalPKfS0_S0_S0_S0_Pf.kd
    .uniform_work_group_size: 1
    .uses_dynamic_stack: false
    .vgpr_count:     96
    .vgpr_spill_count: 0
    .wavefront_size: 64
  - .agpr_count:     0
    .args:
      - .actual_access:  read_only
        .address_space:  global
        .offset:         0
        .size:           8
        .value_kind:     global_buffer
      - .actual_access:  read_only
        .address_space:  global
        .offset:         8
        .size:           8
        .value_kind:     global_buffer
      - .actual_access:  read_only
        .address_space:  global
        .offset:         16
        .size:           8
        .value_kind:     global_buffer
      - .actual_access:  read_only
        .address_space:  global
        .offset:         24
        .size:           8
        .value_kind:     global_buffer
      - .actual_access:  read_only
        .address_space:  global
        .offset:         32
        .size:           8
        .value_kind:     global_buffer
      - .actual_access:  read_only
        .address_space:  global
        .offset:         40
        .size:           8
        .value_kind:     global_buffer
      - .actual_access:  read_only
        .address_space:  global
        .offset:         48
        .size:           8
        .value_kind:     global_buffer
      - .actual_access:  read_only
        .address_space:  global
        .offset:         56
        .size:           8
        .value_kind:     global_buffer
      - .actual_access:  write_only
        .address_space:  global
        .offset:         64
        .size:           8
        .value_kind:     global_buffer
      - .actual_access:  write_only
        .address_space:  global
        .offset:         72
        .size:           8
        .value_kind:     global_buffer
      - .actual_access:  write_only
        .address_space:  global
        .offset:         80
        .size:           8
        .value_kind:     global_buffer
      - .actual_access:  read_only
        .address_space:  global
        .offset:         88
        .size:           8
        .value_kind:     global_buffer
      - .actual_access:  read_only
        .address_space:  global
        .offset:         96
        .size:           8
        .value_kind:     global_buffer
      - .actual_access:  read_only
        .address_space:  global
        .offset:         104
        .size:           8
        .value_kind:     global_buffer
      - .actual_access:  read_only
        .address_space:  global
        .offset:         112
        .size:           8
        .value_kind:     global_buffer
      - .actual_access:  read_only
        .address_space:  global
        .offset:         120
        .size:           8
        .value_kind:     global_buffer
      - .actual_access:  read_only
        .address_space:  global
        .offset:         128
        .size:           8
        .value_kind:     global_buffer
      - .actual_access:  read_only
        .address_space:  global
        .offset:         136
        .size:           8
        .value_kind:     global_buffer
      - .actual_access:  read_only
        .address_space:  global
        .offset:         144
        .size:           8
        .value_kind:     global_buffer
    .group_segment_fixed_size: 29248
    .kernarg_segment_align: 8
    .kernarg_segment_size: 152
    .language:       OpenCL C
    .language_version:
      - 2
      - 0
    .max_flat_workgroup_size: 256
    .name:           _Z7k_layerILi0EEvPKiS1_PKfS3_PKDF16_S3_S5_S5_PDF16_P15HIP_vector_typeIfLj4EES9_S3_S3_S3_S3_S3_S3_PfSA_
    .private_segment_fixed_size: 0
    .sgpr_count:     66
    .sgpr_spill_count: 0
    .symbol:         _Z7k_layerILi0EEvPKiS1_PKfS3_PKDF16_S3_S5_S5_PDF16_P15HIP_vector_typeIfLj4EES9_S3_S3_S3_S3_S3_S3_PfSA_.kd
    .uniform_work_group_size: 1
    .uses_dynamic_stack: false
    .vgpr_count:     86
    .vgpr_spill_count: 0
    .wavefront_size: 64
  - .agpr_count:     0
    .args:
      - .actual_access:  read_only
        .address_space:  global
        .offset:         0
        .size:           8
        .value_kind:     global_buffer
      - .actual_access:  read_only
        .address_space:  global
        .offset:         8
        .size:           8
        .value_kind:     global_buffer
      - .actual_access:  read_only
        .address_space:  global
        .offset:         16
        .size:           8
        .value_kind:     global_buffer
      - .actual_access:  read_only
        .address_space:  global
        .offset:         24
        .size:           8
        .value_kind:     global_buffer
      - .actual_access:  read_only
        .address_space:  global
        .offset:         32
        .size:           8
        .value_kind:     global_buffer
      - .actual_access:  read_only
        .address_space:  global
        .offset:         40
        .size:           8
        .value_kind:     global_buffer
      - .actual_access:  read_only
        .address_space:  global
        .offset:         48
        .size:           8
        .value_kind:     global_buffer
      - .actual_access:  read_only
        .address_space:  global
        .offset:         56
        .size:           8
        .value_kind:     global_buffer
      - .actual_access:  write_only
        .address_space:  global
        .offset:         64
        .size:           8
        .value_kind:     global_buffer
      - .actual_access:  write_only
        .address_space:  global
        .offset:         72
        .size:           8
        .value_kind:     global_buffer
      - .actual_access:  write_only
        .address_space:  global
        .offset:         80
        .size:           8
        .value_kind:     global_buffer
      - .actual_access:  read_only
        .address_space:  global
        .offset:         88
        .size:           8
        .value_kind:     global_buffer
      - .actual_access:  read_only
        .address_space:  global
        .offset:         96
        .size:           8
        .value_kind:     global_buffer
      - .actual_access:  read_only
        .address_space:  global
        .offset:         104
        .size:           8
        .value_kind:     global_buffer
      - .actual_access:  read_only
        .address_space:  global
        .offset:         112
        .size:           8
        .value_kind:     global_buffer
      - .actual_access:  read_only
        .address_space:  global
        .offset:         120
        .size:           8
        .value_kind:     global_buffer
      - .actual_access:  read_only
        .address_space:  global
        .offset:         128
        .size:           8
        .value_kind:     global_buffer
      - .actual_access:  read_only
        .address_space:  global
        .offset:         136
        .size:           8
        .value_kind:     global_buffer
      - .actual_access:  read_only
        .address_space:  global
        .offset:         144
        .size:           8
        .value_kind:     global_buffer
    .group_segment_fixed_size: 21504
    .kernarg_segment_align: 8
    .kernarg_segment_size: 152
    .language:       OpenCL C
    .language_version:
      - 2
      - 0
    .max_flat_workgroup_size: 256
    .name:           _Z7k_layerILi1EEvPKiS1_PKfS3_PKDF16_S3_S5_S5_PDF16_P15HIP_vector_typeIfLj4EES9_S3_S3_S3_S3_S3_S3_PfSA_
    .private_segment_fixed_size: 0
    .sgpr_count:     70
    .sgpr_spill_count: 0
    .symbol:         _Z7k_layerILi1EEvPKiS1_PKfS3_PKDF16_S3_S5_S5_PDF16_P15HIP_vector_typeIfLj4EES9_S3_S3_S3_S3_S3_S3_PfSA_.kd
    .uniform_work_group_size: 1
    .uses_dynamic_stack: false
    .vgpr_count:     96
    .vgpr_spill_count: 0
    .wavefront_size: 64
  - .agpr_count:     0
    .args:
      - .actual_access:  read_only
        .address_space:  global
        .offset:         0
        .size:           8
        .value_kind:     global_buffer
      - .actual_access:  read_only
        .address_space:  global
        .offset:         8
        .size:           8
        .value_kind:     global_buffer
      - .actual_access:  read_only
        .address_space:  global
        .offset:         16
        .size:           8
        .value_kind:     global_buffer
      - .actual_access:  read_only
        .address_space:  global
        .offset:         24
        .size:           8
        .value_kind:     global_buffer
      - .actual_access:  read_only
        .address_space:  global
        .offset:         32
        .size:           8
        .value_kind:     global_buffer
      - .actual_access:  read_only
        .address_space:  global
        .offset:         40
        .size:           8
        .value_kind:     global_buffer
      - .actual_access:  read_only
        .address_space:  global
        .offset:         48
        .size:           8
        .value_kind:     global_buffer
      - .actual_access:  read_only
        .address_space:  global
        .offset:         56
        .size:           8
        .value_kind:     global_buffer
      - .actual_access:  read_only
        .address_space:  global
        .offset:         64
        .size:           8
        .value_kind:     global_buffer
      - .actual_access:  read_only
        .address_space:  global
        .offset:         72
        .size:           8
        .value_kind:     global_buffer
      - .actual_access:  read_only
        .address_space:  global
        .offset:         80
        .size:           8
        .value_kind:     global_buffer
      - .actual_access:  read_only
        .address_space:  global
        .offset:         88
        .size:           8
        .value_kind:     global_buffer
      - .actual_access:  read_only
        .address_space:  global
        .offset:         96
        .size:           8
        .value_kind:     global_buffer
      - .actual_access:  read_only
        .address_space:  global
        .offset:         104
        .size:           8
        .value_kind:     global_buffer
      - .actual_access:  read_only
        .address_space:  global
        .offset:         112
        .size:           8
        .value_kind:     global_buffer
      - .actual_access:  read_only
        .address_space:  global
        .offset:         120
        .size:           8
        .value_kind:     global_buffer
      - .actual_access:  read_only
        .address_space:  global
        .offset:         128
        .size:           8
        .value_kind:     global_buffer
      - .actual_access:  write_only
        .address_space:  global
        .offset:         136
        .size:           8
        .value_kind:     global_buffer
      - .address_space:  global
        .offset:         144
        .size:           8
        .value_kind:     global_buffer
    .group_segment_fixed_size: 19456
    .kernarg_segment_align: 8
    .kernarg_segment_size: 152
    .language:       OpenCL C
    .language_version:
      - 2
      - 0
    .max_flat_workgroup_size: 256
    .name:           _Z7k_layerILi2EEvPKiS1_PKfS3_PKDF16_S3_S5_S5_PDF16_P15HIP_vector_typeIfLj4EES9_S3_S3_S3_S3_S3_S3_PfSA_
    .private_segment_fixed_size: 0
    .sgpr_count:     74
    .sgpr_spill_count: 0
    .symbol:         _Z7k_layerILi2EEvPKiS1_PKfS3_PKDF16_S3_S5_S5_PDF16_P15HIP_vector_typeIfLj4EES9_S3_S3_S3_S3_S3_S3_PfSA_.kd
    .uniform_work_group_size: 1
    .uses_dynamic_stack: false
    .vgpr_count:     110
    .vgpr_spill_count: 0
    .wavefront_size: 64
